# v54 + router-logit MFMA loop of phase K software-pipelined (12 operand pairs in flight, first loads hoisted above the rstd chain)
# speedup vs baseline: 1.0136x; 1.0067x over previous
.LBB0_5125:
	v_add_u32_e32 v2, s40, v28
	v_ashrrev_i32_e32 v3, 31, v2
	v_lshlrev_b64 v[4:5], 7, v[2:3]
	v_lshl_add_u64 v[4:5], v[18:19], 0, v[4:5]
	global_load_dwordx4 v[4:7], v[4:5], off
	v_ashrrev_i32_e32 v25, 31, v24
	v_lshlrev_b64 v[62:63], 12, v[24:25]
	v_lshl_add_u64 v[26:27], v[22:23], 0, v[62:63]
	global_load_dwordx4 v[38:41], v[26:27], off offset:-128
	global_load_dwordx4 v[42:45], v[20:21], off offset:-128
	global_load_dwordx4 v[46:49], v[26:27], off offset:-96
	global_load_dwordx4 v[50:53], v[20:21], off offset:-96
	global_load_dwordx4 v[54:57], v[26:27], off offset:-64
	global_load_dwordx4 v[58:61], v[20:21], off offset:-64
	global_load_dwordx4 v[156:159], v[26:27], off offset:-32
	global_load_dwordx4 v[160:163], v[20:21], off offset:-32
	global_load_dwordx4 v[164:167], v[26:27], off
	global_load_dwordx4 v[168:171], v[20:21], off
	global_load_dwordx4 v[172:175], v[26:27], off offset:32
	global_load_dwordx4 v[176:179], v[20:21], off offset:32
	global_load_dwordx4 v[180:183], v[26:27], off offset:64
	global_load_dwordx4 v[184:187], v[20:21], off offset:64
	global_load_dwordx4 v[188:191], v[26:27], off offset:96
	global_load_dwordx4 v[198:201], v[20:21], off offset:96
	global_load_dwordx4 v[202:205], v[26:27], off offset:128
	global_load_dwordx4 v[206:209], v[20:21], off offset:128
	global_load_dwordx4 v[210:213], v[26:27], off offset:160
	global_load_dwordx4 v[214:217], v[20:21], off offset:160
	global_load_dwordx4 v[242:245], v[26:27], off offset:192
	global_load_dwordx4 v[246:249], v[20:21], off offset:192
	global_load_dwordx4 v[250:253], v[26:27], off offset:224
	global_load_dwordx4 v[230:233], v[20:21], off offset:224
	s_waitcnt vmcnt(24)
	v_add_f32_e32 v0, v4, v5
	v_add_f32_e32 v4, v6, v7
	v_add_f32_e32 v0, v0, v4
	ds_bpermute_b32 v4, v29, v0
	s_waitcnt lgkmcnt(0)
	v_add_f32_e32 v0, v0, v4
	ds_bpermute_b32 v4, v30, v0
	s_waitcnt lgkmcnt(0)
	v_add_f32_e32 v0, v0, v4
	ds_bpermute_b32 v4, v31, v0
	s_and_saveexec_b64 s[6:7], s[2:3]
	s_cbranch_execz .LBB0_5127
	s_waitcnt lgkmcnt(0)
	v_add_f32_e32 v0, v0, v4
	v_fmamk_f32 v0, v0, 0x3a000000, v220
	v_mul_f32_e32 v4, 0x4b800000, v0
	v_cmp_gt_f32_e32 vcc, s65, v0
	v_lshl_add_u64 v[2:3], v[2:3], 2, s[26:27]
	s_nop 0
	v_cndmask_b32_e32 v0, v0, v4, vcc
	v_rsq_f32_e32 v0, v0
	s_nop 0
	v_mul_f32_e32 v4, 0x45800000, v0
	v_cndmask_b32_e32 v0, v0, v4, vcc
	ds_write_b32 v32, v0 offset:49152
	global_store_dword v[2:3], v0, off
.LBB0_5127:
	s_or_b64 exec, exec, s[6:7]
	v_mov_b32_e32 v2, 0
	s_mov_b64 s[6:7], 0
	v_mov_b32_e32 v3, v2
	s_waitcnt lgkmcnt(0)
	v_mov_b32_e32 v4, v2
	v_mov_b32_e32 v5, v2
	v_mov_b32_e32 v6, v2
	v_mov_b32_e32 v7, v2
	v_mov_b32_e32 v8, v2
	v_mov_b32_e32 v9, v2
	v_mov_b32_e32 v10, v2
	v_mov_b32_e32 v11, v2
	v_mov_b32_e32 v12, v2
	v_mov_b32_e32 v13, v2
	v_mov_b32_e32 v14, v2
	v_mov_b32_e32 v15, v2
	v_mov_b32_e32 v16, v2
	v_mov_b32_e32 v17, v2
	s_barrier
	s_waitcnt vmcnt(22)
	v_mfma_f32_32x32x16_bf16 v[2:17], v[38:41], v[42:45], v[2:17]
	global_load_dwordx4 v[38:41], v[26:27], off offset:256
	global_load_dwordx4 v[42:45], v[20:21], off offset:256
	s_waitcnt vmcnt(22)
	v_mfma_f32_32x32x16_bf16 v[2:17], v[46:49], v[50:53], v[2:17]
	global_load_dwordx4 v[46:49], v[26:27], off offset:288
	global_load_dwordx4 v[50:53], v[20:21], off offset:288
	s_waitcnt vmcnt(22)
	v_mfma_f32_32x32x16_bf16 v[2:17], v[54:57], v[58:61], v[2:17]
	global_load_dwordx4 v[54:57], v[26:27], off offset:320
	global_load_dwordx4 v[58:61], v[20:21], off offset:320
	s_waitcnt vmcnt(22)
	v_mfma_f32_32x32x16_bf16 v[2:17], v[156:159], v[160:163], v[2:17]
	global_load_dwordx4 v[156:159], v[26:27], off offset:352
	global_load_dwordx4 v[160:163], v[20:21], off offset:352
	s_waitcnt vmcnt(22)
	v_mfma_f32_32x32x16_bf16 v[2:17], v[164:167], v[168:171], v[2:17]
	global_load_dwordx4 v[164:167], v[26:27], off offset:384
	global_load_dwordx4 v[168:171], v[20:21], off offset:384
	s_waitcnt vmcnt(22)
	v_mfma_f32_32x32x16_bf16 v[2:17], v[172:175], v[176:179], v[2:17]
	global_load_dwordx4 v[172:175], v[26:27], off offset:416
	global_load_dwordx4 v[176:179], v[20:21], off offset:416
	s_waitcnt vmcnt(22)
	v_mfma_f32_32x32x16_bf16 v[2:17], v[180:183], v[184:187], v[2:17]
	global_load_dwordx4 v[180:183], v[26:27], off offset:448
	global_load_dwordx4 v[184:187], v[20:21], off offset:448
	s_waitcnt vmcnt(22)
	v_mfma_f32_32x32x16_bf16 v[2:17], v[188:191], v[198:201], v[2:17]
	global_load_dwordx4 v[188:191], v[26:27], off offset:480
	global_load_dwordx4 v[198:201], v[20:21], off offset:480
	s_waitcnt vmcnt(22)
	v_mfma_f32_32x32x16_bf16 v[2:17], v[202:205], v[206:209], v[2:17]
	global_load_dwordx4 v[202:205], v[26:27], off offset:512
	global_load_dwordx4 v[206:209], v[20:21], off offset:512
	s_waitcnt vmcnt(22)
	v_mfma_f32_32x32x16_bf16 v[2:17], v[210:213], v[214:217], v[2:17]
	global_load_dwordx4 v[210:213], v[26:27], off offset:544
	global_load_dwordx4 v[214:217], v[20:21], off offset:544
	s_waitcnt vmcnt(22)
	v_mfma_f32_32x32x16_bf16 v[2:17], v[242:245], v[246:249], v[2:17]
	global_load_dwordx4 v[242:245], v[26:27], off offset:576
	global_load_dwordx4 v[246:249], v[20:21], off offset:576
	s_waitcnt vmcnt(22)
	v_mfma_f32_32x32x16_bf16 v[2:17], v[250:253], v[230:233], v[2:17]
	global_load_dwordx4 v[250:253], v[26:27], off offset:608
	global_load_dwordx4 v[230:233], v[20:21], off offset:608
	s_waitcnt vmcnt(22)
	v_mfma_f32_32x32x16_bf16 v[2:17], v[38:41], v[42:45], v[2:17]
	global_load_dwordx4 v[38:41], v[26:27], off offset:640
	global_load_dwordx4 v[42:45], v[20:21], off offset:640
	s_waitcnt vmcnt(22)
	v_mfma_f32_32x32x16_bf16 v[2:17], v[46:49], v[50:53], v[2:17]
	global_load_dwordx4 v[46:49], v[26:27], off offset:672
	global_load_dwordx4 v[50:53], v[20:21], off offset:672
	s_waitcnt vmcnt(22)
	v_mfma_f32_32x32x16_bf16 v[2:17], v[54:57], v[58:61], v[2:17]
	global_load_dwordx4 v[54:57], v[26:27], off offset:704
	global_load_dwordx4 v[58:61], v[20:21], off offset:704
	s_waitcnt vmcnt(22)
	v_mfma_f32_32x32x16_bf16 v[2:17], v[156:159], v[160:163], v[2:17]
	global_load_dwordx4 v[156:159], v[26:27], off offset:736
	global_load_dwordx4 v[160:163], v[20:21], off offset:736
	s_waitcnt vmcnt(22)
	v_mfma_f32_32x32x16_bf16 v[2:17], v[164:167], v[168:171], v[2:17]
	global_load_dwordx4 v[164:167], v[26:27], off offset:768
	global_load_dwordx4 v[168:171], v[20:21], off offset:768
	s_waitcnt vmcnt(22)
	v_mfma_f32_32x32x16_bf16 v[2:17], v[172:175], v[176:179], v[2:17]
	global_load_dwordx4 v[172:175], v[26:27], off offset:800
	global_load_dwordx4 v[176:179], v[20:21], off offset:800
	s_waitcnt vmcnt(22)
	v_mfma_f32_32x32x16_bf16 v[2:17], v[180:183], v[184:187], v[2:17]
	global_load_dwordx4 v[180:183], v[26:27], off offset:832
	global_load_dwordx4 v[184:187], v[20:21], off offset:832
	s_waitcnt vmcnt(22)
	v_mfma_f32_32x32x16_bf16 v[2:17], v[188:191], v[198:201], v[2:17]
	global_load_dwordx4 v[188:191], v[26:27], off offset:864
	global_load_dwordx4 v[198:201], v[20:21], off offset:864
	s_waitcnt vmcnt(22)
	v_mfma_f32_32x32x16_bf16 v[2:17], v[202:205], v[206:209], v[2:17]
	s_waitcnt vmcnt(20)
	v_mfma_f32_32x32x16_bf16 v[2:17], v[210:213], v[214:217], v[2:17]
	s_waitcnt vmcnt(18)
	v_mfma_f32_32x32x16_bf16 v[2:17], v[242:245], v[246:249], v[2:17]
	s_waitcnt vmcnt(16)
	v_mfma_f32_32x32x16_bf16 v[2:17], v[250:253], v[230:233], v[2:17]
	s_waitcnt vmcnt(14)
	v_mfma_f32_32x32x16_bf16 v[2:17], v[38:41], v[42:45], v[2:17]
	s_waitcnt vmcnt(12)
	v_mfma_f32_32x32x16_bf16 v[2:17], v[46:49], v[50:53], v[2:17]
	s_waitcnt vmcnt(10)
	v_mfma_f32_32x32x16_bf16 v[2:17], v[54:57], v[58:61], v[2:17]
	s_waitcnt vmcnt(8)
	v_mfma_f32_32x32x16_bf16 v[2:17], v[156:159], v[160:163], v[2:17]
	s_waitcnt vmcnt(6)
	v_mfma_f32_32x32x16_bf16 v[2:17], v[164:167], v[168:171], v[2:17]
	s_waitcnt vmcnt(4)
	v_mfma_f32_32x32x16_bf16 v[2:17], v[172:175], v[176:179], v[2:17]
	s_waitcnt vmcnt(2)
	v_mfma_f32_32x32x16_bf16 v[2:17], v[180:183], v[184:187], v[2:17]
	s_waitcnt vmcnt(0)
	v_mfma_f32_32x32x16_bf16 v[2:17], v[188:191], v[198:201], v[2:17]
	s_and_b64 vcc, exec, s[28:29]
	s_nop 9
	ds_write2st64_b32 v33, v2, v3 offset1:1
	ds_write2st64_b32 v33, v4, v5 offset0:2 offset1:3
	ds_write2st64_b32 v33, v6, v7 offset0:4 offset1:5
	ds_write2st64_b32 v33, v8, v9 offset0:6 offset1:7
	ds_write2st64_b32 v33, v10, v11 offset0:8 offset1:9
	ds_write2st64_b32 v33, v12, v13 offset0:10 offset1:11
	ds_write2st64_b32 v33, v14, v15 offset0:12 offset1:13
	ds_write2st64_b32 v33, v16, v17 offset0:14 offset1:15
	s_waitcnt lgkmcnt(0)
	s_barrier
	s_cbranch_vccz .LBB0_5124
	ds_read_b32 v0, v33
	ds_read_b32 v2, v33 offset:8192
	s_waitcnt lgkmcnt(0)
	v_add_f32_e32 v0, v0, v2
	ds_read_b32 v2, v33 offset:16384
	ds_read_b32 v3, v33 offset:24576
	s_waitcnt lgkmcnt(0)
	v_add_f32_e32 v2, v2, v3
	v_add_f32_e32 v0, v0, v2
	ds_write_b32 v37, v0 offset:32768
	ds_read_b32 v0, v33 offset:256
	ds_read_b32 v2, v33 offset:8448
	s_waitcnt lgkmcnt(0)
	v_add_f32_e32 v0, v0, v2
	ds_read_b32 v2, v33 offset:16640
	ds_read_b32 v3, v33 offset:24832
	s_waitcnt lgkmcnt(0)
	v_add_f32_e32 v2, v2, v3
	v_add_f32_e32 v0, v0, v2
	ds_write_b32 v37, v0 offset:32900
	ds_read_b32 v0, v33 offset:512
	ds_read_b32 v2, v33 offset:8704
	s_waitcnt lgkmcnt(0)
	v_add_f32_e32 v0, v0, v2
	ds_read_b32 v2, v33 offset:16896
	ds_read_b32 v3, v33 offset:25088
	s_waitcnt lgkmcnt(0)
	v_add_f32_e32 v2, v2, v3
	v_add_f32_e32 v0, v0, v2
	ds_write_b32 v37, v0 offset:33032
	ds_read_b32 v0, v33 offset:768
	ds_read_b32 v2, v33 offset:8960
	s_waitcnt lgkmcnt(0)
	v_add_f32_e32 v0, v0, v2
	ds_read_b32 v2, v33 offset:17152
	ds_read_b32 v3, v33 offset:25344
	s_waitcnt lgkmcnt(0)
	v_add_f32_e32 v2, v2, v3
	v_add_f32_e32 v0, v0, v2
	ds_write_b32 v37, v0 offset:33164
	ds_read_b32 v0, v33 offset:1024
	ds_read_b32 v2, v33 offset:9216
	s_waitcnt lgkmcnt(0)
	v_add_f32_e32 v0, v0, v2
	ds_read_b32 v2, v33 offset:17408
	ds_read_b32 v3, v33 offset:25600
	s_waitcnt lgkmcnt(0)
	v_add_f32_e32 v2, v2, v3
	v_add_f32_e32 v0, v0, v2
	ds_write_b32 v37, v0 offset:33824
	ds_read_b32 v0, v33 offset:1280
	ds_read_b32 v2, v33 offset:9472
	s_waitcnt lgkmcnt(0)
	v_add_f32_e32 v0, v0, v2
	ds_read_b32 v2, v33 offset:17664
	ds_read_b32 v3, v33 offset:25856
	s_waitcnt lgkmcnt(0)
	v_add_f32_e32 v2, v2, v3
	v_add_f32_e32 v0, v0, v2
	ds_write_b32 v37, v0 offset:33956
	ds_read_b32 v0, v33 offset:1536
	ds_read_b32 v2, v33 offset:9728
	s_waitcnt lgkmcnt(0)
	v_add_f32_e32 v0, v0, v2
	ds_read_b32 v2, v33 offset:17920
	ds_read_b32 v3, v33 offset:26112
	s_waitcnt lgkmcnt(0)
	v_add_f32_e32 v2, v2, v3
	v_add_f32_e32 v0, v0, v2
	ds_write_b32 v37, v0 offset:34088
	ds_read_b32 v0, v33 offset:1792
	ds_read_b32 v2, v33 offset:9984
	s_waitcnt lgkmcnt(0)
	v_add_f32_e32 v0, v0, v2
	ds_read_b32 v2, v33 offset:18176
	ds_read_b32 v3, v33 offset:26368
	s_waitcnt lgkmcnt(0)
	v_add_f32_e32 v2, v2, v3
	v_add_f32_e32 v0, v0, v2
	ds_write_b32 v37, v0 offset:34220
	ds_read_b32 v0, v33 offset:2048
	ds_read_b32 v2, v33 offset:10240
	s_waitcnt lgkmcnt(0)
	v_add_f32_e32 v0, v0, v2
	ds_read_b32 v2, v33 offset:18432
	ds_read_b32 v3, v33 offset:26624
	s_waitcnt lgkmcnt(0)
	v_add_f32_e32 v2, v2, v3
	v_add_f32_e32 v0, v0, v2
	ds_write_b32 v37, v0 offset:34880
	ds_read_b32 v0, v33 offset:2304
	ds_read_b32 v2, v33 offset:10496
	s_waitcnt lgkmcnt(0)
	v_add_f32_e32 v0, v0, v2
	ds_read_b32 v2, v33 offset:18688
	ds_read_b32 v3, v33 offset:26880
	s_waitcnt lgkmcnt(0)
	v_add_f32_e32 v2, v2, v3
	v_add_f32_e32 v0, v0, v2
	ds_write_b32 v37, v0 offset:35012
	ds_read_b32 v0, v33 offset:2560
	ds_read_b32 v2, v33 offset:10752
	s_waitcnt lgkmcnt(0)
	v_add_f32_e32 v0, v0, v2
	ds_read_b32 v2, v33 offset:18944
	ds_read_b32 v3, v33 offset:27136
	s_waitcnt lgkmcnt(0)
	v_add_f32_e32 v2, v2, v3
	v_add_f32_e32 v0, v0, v2
	ds_write_b32 v37, v0 offset:35144
	ds_read_b32 v0, v33 offset:2816
	ds_read_b32 v2, v33 offset:11008
	s_waitcnt lgkmcnt(0)
	v_add_f32_e32 v0, v0, v2
	ds_read_b32 v2, v33 offset:19200
	ds_read_b32 v3, v33 offset:27392
	s_waitcnt lgkmcnt(0)
	v_add_f32_e32 v2, v2, v3
	v_add_f32_e32 v0, v0, v2
	ds_write_b32 v37, v0 offset:35276
	ds_read_b32 v0, v33 offset:3072
	ds_read_b32 v2, v33 offset:11264
	s_waitcnt lgkmcnt(0)
	v_add_f32_e32 v0, v0, v2
	ds_read_b32 v2, v33 offset:19456
	ds_read_b32 v3, v33 offset:27648
	s_waitcnt lgkmcnt(0)
	v_add_f32_e32 v2, v2, v3
	v_add_f32_e32 v0, v0, v2
	ds_write_b32 v37, v0 offset:35936
	ds_read_b32 v0, v33 offset:3328
	ds_read_b32 v2, v33 offset:11520
	s_waitcnt lgkmcnt(0)
	v_add_f32_e32 v0, v0, v2
	ds_read_b32 v2, v33 offset:19712
	ds_read_b32 v3, v33 offset:27904
	s_waitcnt lgkmcnt(0)
	v_add_f32_e32 v2, v2, v3
	v_add_f32_e32 v0, v0, v2
	ds_write_b32 v37, v0 offset:36068
	ds_read_b32 v0, v33 offset:3584
	ds_read_b32 v2, v33 offset:11776
	s_waitcnt lgkmcnt(0)
	v_add_f32_e32 v0, v0, v2
	ds_read_b32 v2, v33 offset:19968
	ds_read_b32 v3, v33 offset:28160
	s_waitcnt lgkmcnt(0)
	v_add_f32_e32 v2, v2, v3
	v_add_f32_e32 v0, v0, v2
	ds_write_b32 v37, v0 offset:36200
	ds_read_b32 v0, v33 offset:3840
	ds_read_b32 v2, v33 offset:12032
	s_waitcnt lgkmcnt(0)
	v_add_f32_e32 v0, v0, v2
	ds_read_b32 v2, v33 offset:20224
	ds_read_b32 v3, v33 offset:28416
	s_waitcnt lgkmcnt(0)
	v_add_f32_e32 v2, v2, v3
	v_add_f32_e32 v0, v0, v2
	ds_write_b32 v37, v0 offset:36332
	s_waitcnt lgkmcnt(0)
	s_and_saveexec_b64 s[38:39], s[4:5]
	s_cbranch_execz .LBB0_5123
	global_load_dwordx4 v[2:5], v1, s[18:19]
	v_add_u32_e32 v0, 0x8000, v35
	ds_read_b32 v10, v36 offset:49152
	ds_read2_b32 v[6:7], v0 offset1:1
	v_add_u32_e32 v0, 0x8008, v35
	s_mov_b32 s14, 0xff800000
	s_waitcnt vmcnt(0) lgkmcnt(0)
	v_pk_fma_f32 v[2:3], v[10:11], v[6:7], v[2:3] op_sel_hi:[0,1,1]
	ds_read2_b32 v[6:7], v0 offset1:1
	v_cmp_gt_f32_e64 s[6:7], v3, v2
	s_waitcnt lgkmcnt(0)
	v_fma_f32 v11, v10, v6, v4
	v_cndmask_b32_e64 v0, v2, v3, s[6:7]
	v_cmp_gt_f32_e64 s[8:9], v11, v0
	v_fmac_f32_e32 v5, v10, v7
	s_nop 0
	v_cndmask_b32_e64 v13, v0, v11, s[8:9]
	v_cndmask_b32_e64 v0, 0, 4, s[6:7]
	v_cmp_gt_f32_e32 vcc, v5, v13
	v_cndmask_b32_e64 v0, v0, 8, s[8:9]
	s_nop 0
	v_cndmask_b32_e64 v0, v0, 12, vcc
	v_lshlrev_b32_e32 v4, 2, v0
	v_add_u32_e32 v12, v35, v4
	v_add_u32_e32 v6, 0x8010, v12
	ds_read2_b32 v[14:15], v6 offset1:1
	global_load_dwordx4 v[6:9], v4, s[20:21]
	v_add_u32_e32 v4, 0x8018, v12
	s_waitcnt vmcnt(0) lgkmcnt(0)
	v_pk_fma_f32 v[14:15], v[10:11], v[14:15], v[6:7] op_sel_hi:[0,1,1]
	ds_read2_b32 v[6:7], v4 offset1:1
	v_cmp_gt_f32_e64 s[6:7], v15, v14
	v_cmp_nlg_f32_e64 s[14:15], s14, v14
	s_waitcnt lgkmcnt(0)
	v_fma_f32 v8, v10, v6, v8
	v_cndmask_b32_e64 v4, v14, v15, s[6:7]
	v_cmp_ngt_f32_e64 s[8:9], v8, v4
	v_fmac_f32_e32 v9, v10, v7
	v_cndmask_b32_e64 v7, 0, 1, s[6:7]
	v_cndmask_b32_e64 v6, v8, v4, s[8:9]
	v_cndmask_b32_e64 v4, 2, v7, s[8:9]
	v_cmp_gt_f32_e64 s[10:11], v9, v6
	v_cmp_ngt_f32_e64 s[6:7], v9, v6
	s_nop 0
	v_cndmask_b32_e64 v4, v4, 3, s[10:11]
	v_cmp_eq_u32_e64 s[12:13], 0, v4
	s_or_b64 s[12:13], s[12:13], s[14:15]
	s_or_b64 s[10:11], s[10:11], s[8:9]
	v_cndmask_b32_e64 v7, v14, v240, s[12:13]
	v_cndmask_b32_e64 v12, 0, -1, s[12:13]
	v_cmp_ne_u32_e64 s[12:13], 1, v4
	v_cmp_gt_f32_e64 s[14:15], v15, v7
	s_and_b64 s[12:13], s[12:13], s[14:15]
	v_cndmask_b32_e64 v7, v7, v15, s[12:13]
	v_cmp_gt_f32_e64 s[8:9], v8, v7
	v_cndmask_b32_e64 v12, v12, 1, s[12:13]
	s_and_b64 s[8:9], s[10:11], s[8:9]
	v_cndmask_b32_e64 v7, v7, v8, s[8:9]
	v_cndmask_b32_e64 v12, v12, 2, s[8:9]
	s_and_saveexec_b64 s[8:9], s[6:7]
	s_cbranch_execz .LBB0_5122
	v_cmp_gt_f32_e64 s[6:7], v9, v7
	s_and_saveexec_b64 s[10:11], s[6:7]
	s_cbranch_execz .LBB0_5121
	v_mov_b32_e32 v12, 3
	v_mov_b32_e32 v7, v9
	s_branch .LBB0_5121
